# deferred conversion: P4b slot 2 items/wave + P5/P14 slots 3 items/wave (20.6% of the MoE conversion)
# baseline (speedup 1.0000x reference)
; #define LAS __attribute__((address_space(3)))
; __device__ __forceinline__ int tidx() { int t = threadIdx.x; asm volatile("" : "+v"(t)); return t; }
; __device__ __forceinline__ void phase_cvt_moe(LAS unsigned char* lds, const CvtMoe a) {
;     const int tid_ = tidx(), wave = tid_ >> 6, lane = tid_ & 63;
;     LAS float* scr = (LAS float*)(lds + wave * CVT_SCR);
;     const int gw = blockIdx.x * 8 + wave, NGW = gridDim.x * 8;
;     constexpr int IG = (D / 64) * (FF / 64), ID = (FF / 64) * (D / 64);
;     for (int it = gw; it < 2 * NE * (2 * IG + ID); it += NGW) {
;         const int e = it / (2 * IG + ID); int r = it % (2 * IG + ID);
;         if (r < 2 * IG) { const int up = r / IG; r %= IG; const int nblk = FF / 64, kb = r / nblk, nb = r % nblk, n0 = nb * 64;
;             cvt_item((up ? a.wu : a.wg) + (size_t)e * D * FF, D, FF, a.gu + (size_t)e * 2 * FF * D, (n0 / 128) * 256 + up * 128 + (n0 % 128), kb * 64, n0, scr, lane); }
;         else { r -= 2 * IG; const int nblk = D / 64, kb = r / nblk, nb = r % nblk; cvt_item(a.wd + (size_t)e * FF * D, FF, D, a.dn + (size_t)e * D * FF, nb * 64, kb * 64, nb * 64, scr, lane); }
;     }
.LBB0_55:
	s_or_b64 exec, exec, s[4:5]
	s_add_u32 s4, s90, 0x30a13600
	s_addc_u32 s5, s91, 0
	v_writelane_b32 v250, s4, 6
	v_mov_b32_e32 v4, v0
	s_nop 0
	v_writelane_b32 v250, s5, 7
	s_add_u32 s4, s90, 0x46a13600
	s_addc_u32 s5, s91, 0
	v_writelane_b32 v250, s4, 8
	v_ashrrev_i32_e32 v2, 6, v4
	v_add_u32_e32 v5, s14, v2
	v_writelane_b32 v250, s5, 9
	s_mov_b32 s4, 0xd180
	v_cmp_gt_i32_e32 vcc, s4, v5
	s_and_saveexec_b64 s[4:5], vcc
	s_cbranch_execz .LBB0_62
	s_movk_i32 s6, 0x4100
	v_mul_lo_u32 v3, v2, s6
	v_add_u32_e32 v8, 0, v3
	v_lshlrev_b32_e32 v3, 2, v4
	v_bfe_u32 v6, v4, 4, 2
	v_and_b32_e32 v44, 60, v3
	v_bfe_u32 v7, v4, 3, 3
	v_lshlrev_b32_e32 v4, 3, v4
	v_lshl_add_u32 v20, v44, 2, v8
	v_mul_u32_u24_e32 v21, 0x104, v6
	v_and_b32_e32 v4, 56, v4
	v_mul_u32_u24_e32 v9, 0x104, v4
	v_lshlrev_b32_e32 v10, 2, v7
	v_lshlrev_b32_e32 v16, 2, v2
	v_add_u32_e32 v20, v20, v21
	v_mov_b32_e32 v3, 0
	v_add3_u32 v8, v8, v9, v10
	v_or_b32_e32 v9, 8, v7
	v_or_b32_e32 v10, 16, v7
	v_or_b32_e32 v11, 24, v7
	v_or_b32_e32 v12, 32, v7
	v_or_b32_e32 v13, 40, v7
	v_or_b32_e32 v14, 48, v7
	v_or_b32_e32 v15, 56, v7
	v_lshl_add_u32 v16, s2, 5, v16
	v_lshlrev_b32_e32 v17, 2, v1
	v_lshl_add_u32 v18, v2, 6, s3
	v_lshlrev_b32_e32 v19, 6, v1
	s_mov_b64 s[6:7], 0
	s_mov_b32 s3, 0x3e0f83e1
	s_movk_i32 s10, 0x57f
	s_mov_b32 s11, 0xb00000
	v_add_u32_e32 v21, 0x410, v20
	v_add_u32_e32 v22, 0x418, v20
	v_add_u32_e32 v23, 0x820, v20
	v_add_u32_e32 v24, 0x828, v20
	v_add_u32_e32 v25, 0xc30, v20
	v_add_u32_e32 v26, 0xc38, v20
	v_add_u32_e32 v27, 0x1040, v20
	v_add_u32_e32 v28, 0x1048, v20
	v_add_u32_e32 v29, 0x1450, v20
	v_add_u32_e32 v30, 0x1458, v20
	v_add_u32_e32 v31, 0x1860, v20
	v_add_u32_e32 v32, 0x1868, v20
	v_add_u32_e32 v33, 0x1c70, v20
	v_add_u32_e32 v34, 0x1c78, v20
	v_add_u32_e32 v35, 0x2080, v20
	v_add_u32_e32 v36, 0x2088, v20
	v_add_u32_e32 v37, 0x2490, v20
	v_add_u32_e32 v38, 0x2498, v20
	v_add_u32_e32 v39, 0x28a0, v20
	v_add_u32_e32 v40, 0x28a8, v20
	v_add_u32_e32 v41, 0x2cb0, v20
	v_add_u32_e32 v42, 0x2cb8, v20
	s_movk_i32 s12, 0xba3
	s_mov_b32 s13, 0xb000
	s_mov_b32 s14, 0x16000
	s_mov_b32 s15, 0x21000
	s_mov_b32 s16, 0x2c000
	s_mov_b32 s17, 0x37000
	s_mov_b32 s18, 0x42000
	s_mov_b32 s19, 0x4d000
	s_mov_b32 s20, 0x58000
	s_mov_b32 s21, 0x63000
	s_mov_b32 s22, 0x6e000
	s_mov_b32 s23, 0x79000
	s_mov_b32 s24, 0x84000
	s_mov_b32 s25, 0x8f000
	s_mov_b32 s26, 0x9a000
	s_mov_b32 s27, 0xa5000
	s_mov_b32 s28, 0xd17f
	v_lshlrev_b32_e32 v2, 2, v44
	v_add_u32_e32 v43, 0x30c0, v20
	v_add_u32_e32 v44, 0x30c8, v20
	v_add_u32_e32 v45, 0x34d0, v20
	v_add_u32_e32 v46, 0x34d8, v20
	v_mov_b32_e32 v47, 6
	v_mov_b32_e32 v48, 1
	v_mov_b32_e32 v49, 8
	v_mov_b32_e32 v50, 7
	s_branch .LBB0_58

; #define LAS __attribute__((address_space(3)))
; __device__ __forceinline__ int tidx() { int t = threadIdx.x; asm volatile("" : "+v"(t)); return t; }
; __device__ __forceinline__ void phase_cvt_moe(LAS unsigned char* lds, const CvtMoe a) {
;     const int tid_ = tidx(), wave = tid_ >> 6, lane = tid_ & 63;
;     LAS float* scr = (LAS float*)(lds + wave * CVT_SCR);
;     const int gw = blockIdx.x * 8 + wave, NGW = gridDim.x * 8;
;     constexpr int IG = (D / 64) * (FF / 64), ID = (FF / 64) * (D / 64);
;     for (int it = gw; it < 2 * NE * (2 * IG + ID); it += NGW) {
;         const int e = it / (2 * IG + ID); int r = it % (2 * IG + ID);
;         if (r < 2 * IG) { const int up = r / IG; r %= IG; const int nblk = FF / 64, kb = r / nblk, nb = r % nblk, n0 = nb * 64;
.Lcvp4b_entry:
	s_sub_i32 s0, s94, 8
	v_readlane_b32 s2, v250, 26
	v_readlane_b32 s3, v250, 27
	s_nop 3
	s_sub_u32 s2, s2, 0xc0
	s_subb_u32 s3, s3, 0
	s_load_dwordx2 s[38:39], s[2:3], 0x90
	s_load_dwordx2 s[40:41], s[2:3], 0x98
	s_load_dwordx2 s[34:35], s[2:3], 0xa0
	s_lshl_b32 s0, s0, 3
	s_add_i32 s0, s0, 0xd180
	v_mov_b32_e32 v131, 0x7c0
	s_waitcnt lgkmcnt(0)
	s_add_u32 s4, s90, 0x30a13600
	s_addc_u32 s5, s91, 0
	v_writelane_b32 v250, s4, 6
	v_mov_b32_e32 v130, v0
	s_nop 0
	v_writelane_b32 v250, s5, 7
	s_add_u32 s4, s90, 0x46a13600
	s_addc_u32 s5, s91, 0
	v_writelane_b32 v250, s4, 8
	v_ashrrev_i32_e32 v2, 6, v130
	v_add_u32_e32 v5, s0, v2
	v_writelane_b32 v250, s5, 9
	s_mov_b32 s4, 0xe100
	v_cmp_gt_i32_e32 vcc, s4, v5
	s_and_saveexec_b64 s[4:5], vcc
	s_cbranch_execz .Lcvp4b_62
	s_movk_i32 s6, 0x4100
	v_mul_lo_u32 v3, v2, s6
	v_add_u32_e32 v8, 0, v3
	v_lshlrev_b32_e32 v3, 2, v130
	v_bfe_u32 v6, v130, 4, 2
	v_and_b32_e32 v44, 60, v3
	v_bfe_u32 v7, v130, 3, 3
	v_lshlrev_b32_e32 v130, 3, v130
	v_lshl_add_u32 v20, v44, 2, v8
	v_mul_u32_u24_e32 v21, 0x104, v6
	v_and_b32_e32 v130, 56, v130
	v_mul_u32_u24_e32 v9, 0x104, v130
	v_lshlrev_b32_e32 v10, 2, v7
	v_lshlrev_b32_e32 v16, 2, v2
	v_add_u32_e32 v20, v20, v21
	v_mov_b32_e32 v3, 0
	v_add3_u32 v8, v8, v9, v10
	v_or_b32_e32 v9, 8, v7
	v_or_b32_e32 v10, 16, v7
	v_or_b32_e32 v11, 24, v7
	v_or_b32_e32 v12, 32, v7
	v_or_b32_e32 v13, 40, v7
	v_or_b32_e32 v14, 48, v7
	v_or_b32_e32 v15, 56, v7
	v_lshlrev_b32_e32 v16, 2, v5
	v_lshlrev_b32_e32 v17, 2, v131
	v_lshlrev_b32_e32 v18, 6, v5
	v_lshlrev_b32_e32 v19, 6, v131
	s_mov_b64 s[6:7], 0
	s_mov_b32 s3, 0x3e0f83e1
	s_movk_i32 s10, 0x57f
	s_mov_b32 s11, 0xb00000
	v_add_u32_e32 v21, 0x410, v20
	v_add_u32_e32 v22, 0x418, v20
	v_add_u32_e32 v23, 0x820, v20
	v_add_u32_e32 v24, 0x828, v20
	v_add_u32_e32 v25, 0xc30, v20
	v_add_u32_e32 v26, 0xc38, v20
	v_add_u32_e32 v27, 0x1040, v20
	v_add_u32_e32 v28, 0x1048, v20
	v_add_u32_e32 v29, 0x1450, v20
	v_add_u32_e32 v30, 0x1458, v20
	v_add_u32_e32 v31, 0x1860, v20
	v_add_u32_e32 v32, 0x1868, v20
	v_add_u32_e32 v33, 0x1c70, v20
	v_add_u32_e32 v34, 0x1c78, v20
	v_add_u32_e32 v35, 0x2080, v20
	v_add_u32_e32 v36, 0x2088, v20
	v_add_u32_e32 v37, 0x2490, v20
	v_add_u32_e32 v38, 0x2498, v20
	v_add_u32_e32 v39, 0x28a0, v20
	v_add_u32_e32 v40, 0x28a8, v20
	v_add_u32_e32 v41, 0x2cb0, v20
	v_add_u32_e32 v42, 0x2cb8, v20
	s_movk_i32 s64, 0xba3
	s_mov_b32 s65, 0xb000
	s_mov_b32 s66, 0x16000
	s_mov_b32 s67, 0x21000
	s_mov_b32 s16, 0x2c000
	s_mov_b32 s68, 0x37000
	s_mov_b32 s69, 0x42000
	s_mov_b32 s19, 0x4d000
	s_mov_b32 s20, 0x58000
	s_mov_b32 s21, 0x63000
	s_mov_b32 s70, 0x6e000
	s_mov_b32 s23, 0x79000
	s_mov_b32 s24, 0x84000
	s_mov_b32 s25, 0x8f000
	s_mov_b32 s26, 0x9a000
	s_mov_b32 s27, 0xa5000
	s_mov_b32 s71, 0xe0ff
	v_lshlrev_b32_e32 v2, 2, v44
	v_add_u32_e32 v43, 0x30c0, v20
	v_add_u32_e32 v44, 0x30c8, v20
	v_add_u32_e32 v45, 0x34d0, v20
	v_add_u32_e32 v46, 0x34d8, v20
	v_mov_b32_e32 v47, 6
	v_mov_b32_e32 v132, 1
	v_mov_b32_e32 v133, 8
	v_mov_b32_e32 v134, 7
	s_branch .Lcvp4b_58
